# re-measure: spread attention pool counters (4 KiB stride) + nt hint on SEL index stores
# speedup vs baseline: 1.0473x; 1.0048x over previous
.LBB0_457:
	v_cndmask_b32_e64 v136, v1, v2, s[38:39]
	v_cmp_gt_u32_e32 vcc, s35, v136
	s_and_saveexec_b64 s[28:29], vcc
	s_cbranch_execz .LBB0_456
	v_ffbl_b32_e32 v3, v0
	v_add_u32_e32 v3, v3, v5
	v_lshl_add_u64 v[6:7], v[136:137], 1, s[10:11]
	global_store_short v[6:7], v3, off nt
	s_branch .LBB0_456

.LBB0_464:
	v_ashrrev_i32_e32 v15, 31, v0
	v_mov_b32_e32 v14, v0
	v_add_u32_e32 v6, -4, v6
	v_ashrrev_i32_e32 v9, 31, v3
	v_mov_b32_e32 v8, v3
	v_ashrrev_i32_e32 v11, 31, v2
	v_mov_b32_e32 v10, v2
	v_ashrrev_i32_e32 v13, 31, v1
	v_mov_b32_e32 v12, v1
	v_lshl_add_u64 v[14:15], v[14:15], 1, s[10:11]
	v_cmp_eq_u32_e32 vcc, 0, v6
	v_lshl_add_u64 v[12:13], v[12:13], 1, s[10:11]
	v_lshl_add_u64 v[10:11], v[10:11], 1, s[10:11]
	v_lshl_add_u64 v[8:9], v[8:9], 1, s[10:11]
	global_store_short v[14:15], v0, off nt
	global_store_short v[12:13], v1, off nt
	global_store_short v[10:11], v2, off nt
	global_store_short v[8:9], v3, off nt
	v_add_u32_e32 v3, 0x100, v3
	v_add_u32_e32 v2, 0x100, v2
	v_add_u32_e32 v1, 0x100, v1
	s_or_b64 s[28:29], vcc, s[28:29]
	v_add_u32_e32 v0, 0x100, v0
	s_andn2_b64 exec, exec, s[28:29]
	s_cbranch_execnz .LBB0_464
	s_or_b64 exec, exec, s[28:29]
	v_cmp_ne_u32_e32 vcc, v5, v4
	s_mov_b64 s[10:11], 0
	s_and_saveexec_b64 s[28:29], vcc
	v_lshl_add_u32 v0, v4, 6, v114
	v_ashrrev_i32_e32 v1, 31, v0
	s_mov_b64 s[10:11], exec
	v_mov_b64_e32 v[2:3], v[0:1]
	s_or_b64 exec, exec, s[28:29]
	s_orn2_b64 s[28:29], s[10:11], exec

.LBB0_470:
	global_store_short v[2:3], v0, off nt
	v_add_u32_e32 v0, 64, v0
	v_cmp_lt_i32_e32 vcc, s6, v0
	s_or_b64 s[8:9], vcc, s[8:9]
	v_lshl_add_u64 v[2:3], v[2:3], 0, s[24:25]
	s_andn2_b64 exec, exec, s[8:9]
	s_cbranch_execnz .LBB0_470
	s_branch .LBB0_406
